# speedup vs baseline: 1.0571x; 1.0090x over previous
_Z6k_gemmPKfS0_PK15HIP_vector_typeIjLj4EEPDF16_PKh:
	s_load_dwordx4 s[20:23], s[0:1], 0x0
	s_load_dwordx4 s[4:7], s[0:1], 0x10
	s_load_dwordx2 s[38:39], s[0:1], 0x20
	v_readfirstlane_b32 s8, v0
	v_and_b32_e32 v1, 63, v0
	s_nop 3
	s_lshr_b32 s8, s8, 6
	s_and_b32 s40, s2, 7
	s_lshr_b32 s41, s2, 3
	s_mul_i32 s18, s40, 0x187
	s_min_u32 s19, s18, 0xaae
	s_add_i32 s18, s18, s41
	s_sub_i32 s33, s19, s18
	s_addk_i32 s33, 0x1c6
	s_ashr_i32 s9, s33, 6
	s_max_i32 s9, s9, 0
	s_cmp_eq_u32 s9, 0
	s_cbranch_scc1 .Lg_end
	s_add_i32 s11, s9, 4
	s_lshl_b32 s18, s18, 4
	s_lshl_b32 s19, s8, 2
	s_add_i32 s33, s18, s19
	s_mul_i32 s12, s33, 0x4b0
	s_lshl_b32 s32, s18, 8
	s_sub_u32 s32, s32, 0x100000
	s_mov_b32 s10, 0
	v_lshl_add_u32 v253, v1, 10, s33
	v_mov_b32_e32 v247, 0
	v_cmp_gt_i32_e32 vcc, s9, v1
	s_mov_b32 s18, 0xc350
	v_cmp_gt_i32_e64 s[36:37], s18, v253
	s_and_b64 vcc, vcc, s[36:37]
	s_waitcnt lgkmcnt(0)
	s_and_saveexec_b64 s[36:37], vcc
	global_load_dword v247, v253, s[38:39]
	s_mov_b64 exec, s[36:37]
	s_mov_b32 s24, s22
	s_and_b32 s25, s23, 0xffff
	s_mov_b32 s26, 0x3938700
	s_mov_b32 s27, 0x20000
	s_and_b32 s21, s21, 0xffff
	s_mov_b32 s22, 0x3938700
	s_mov_b32 s23, 0x20000
	s_mov_b32 s28, s6
	s_and_b32 s29, s7, 0xffff
	s_mov_b32 s30, 0xc35000
	s_mov_b32 s31, 0x20000
	v_lshlrev_b32_e32 v238, 4, v1
	v_mul_u32_u24_e32 v253, 0x1746, v1
	v_lshrrev_b32_e32 v253, 16, v253
	v_min_u32_e32 v253, 3, v253
	v_mul_u32_u24_e32 v254, 11, v253
	v_sub_u32_e32 v254, v1, v254
	v_lshlrev_b32_e32 v240, 3, v253
	v_mul_u32_u24_e32 v249, 0x4b0, v253
	v_lshl_add_u32 v249, v254, 4, v249
	v_add_u32_e32 v249, 0x400, v249
	v_mov_b32_e32 v255, 0x80000000
	v_cmp_gt_u32_e64 s[34:35], 44, v1
	s_nop 1
	v_cndmask_b32_e64 v239, v255, v249, s[34:35]
	v_lshl_add_u32 v250, s8, 2, v253
	v_mul_u32_u24_e32 v250, 0x4e0, v250
	v_lshl_add_u32 v250, v254, 3, v250
	v_add_u32_e32 v242, 0x200, v250
	s_mul_i32 s18, s8, 0x1380
	v_lshl_add_u32 v241, v1, 3, s18
	v_and_b32_e32 v249, 15, v1
	v_lshrrev_b32_e32 v250, 4, v1
	v_mul_u32_u24_e32 v243, 0x4e0, v249
	v_lshl_add_u32 v243, v250, 4, v243
	v_mul_u32_u24_e32 v244, 0x440, v250
	v_lshl_add_u32 v244, v249, 1, v244
	s_lshl_b32 s18, s8, 6
	s_add_i32 s18, s18, 39936
	v_add_u32_e32 v244, s18, v244
	v_lshrrev_b32_e32 v249, 4, v0
	v_and_b32_e32 v250, 15, v0
	v_mul_u32_u24_e32 v245, 0x110, v249
	v_lshl_add_u32 v245, v250, 4, v245
	v_add_u32_e32 v245, 39936, v245
	v_lshlrev_b32_e32 v246, 8, v249
	v_lshl_add_u32 v246, v250, 4, v246
	s_lshl_b32 s18, s8, 12
	s_add_i32 s18, s18, 48640
	v_lshl_add_u32 v248, v1, 4, s18
	v_cmp_gt_u32_e32 vcc, 32, v0
	s_and_saveexec_b64 s[36:37], vcc
	v_mul_u32_u24_e32 v251, 0x4e00, v249
	v_mul_u32_u24_e32 v252, 0x4e0, v250
	v_add_u32_e32 v254, v251, v252
	v_mov_b32_e32 v250, 0
	v_mov_b32_e32 v251, 0
	v_mov_b32_e32 v252, 0
	v_mov_b32_e32 v253, 0
	ds_write_b128 v254, v[250:253] offset:1200
	s_mov_b64 exec, s[36:37]
	s_lshl_b32 s18, s8, 11
	v_lshl_add_u32 v253, v1, 4, s18
	v_add_u32_e32 v254, 0x22000, v253
	global_load_dwordx4 v[178:181], v254, s[4:5]
	global_load_dwordx4 v[182:185], v254, s[4:5] offset:1024
	v_add_u32_e32 v254, 0x2000, v254
	global_load_dwordx4 v[186:189], v254, s[4:5]
	global_load_dwordx4 v[190:193], v254, s[4:5] offset:1024
	v_mov_b32_e32 v236, v253
	s_waitcnt vmcnt(4)
	v_readlane_b32 s13, v247, s10
	s_add_u32 s14, s12, 0x4b0
	s_add_u32 s15, s12, 0x960
	s_add_u32 s16, s12, 0xe10
	s_nop 1
	s_and_b32 s18, s13, 0xff
	s_cmp_eq_u32 s18, 1
	s_cselect_b32 s42, s12, 0x80000000
	s_and_b32 s18, s13, 0xff00
	s_cmp_eq_u32 s18, 0x100
	s_cselect_b32 s14, s14, 0x80000000
	s_and_b32 s18, s13, 0xff0000
	s_cmp_eq_u32 s18, 0x10000
	s_cselect_b32 s15, s15, 0x80000000
	s_and_b32 s18, s13, 0xff000000
	s_cmp_eq_u32 s18, 0x1000000
	s_cselect_b32 s16, s16, 0x80000000
	v_lshrrev_b32_e64 v249, v240, s13
	v_and_b32_e32 v249, 0xff, v249
	v_cmp_eq_u32_e32 vcc, 1, v249
	s_nop 1
	v_cndmask_b32_e32 v254, v255, v239, vcc
	buffer_load_dwordx4 v[138:141], v238, s[20:23], s42 offen nt
	buffer_load_dwordx4 v[142:145], v238, s[24:27], s42 offen nt
	buffer_load_dwordx4 v[146:149], v238, s[20:23], s14 offen nt
	buffer_load_dwordx4 v[150:153], v238, s[24:27], s14 offen nt
	buffer_load_dwordx4 v[154:157], v238, s[20:23], s15 offen nt
	buffer_load_dwordx4 v[158:161], v238, s[24:27], s15 offen nt
	buffer_load_dwordx4 v[162:165], v238, s[20:23], s16 offen nt
	buffer_load_dwordx4 v[166:169], v238, s[24:27], s16 offen nt
	buffer_load_dwordx4 v[170:173], v254, s[20:23], s12 offen nt
	buffer_load_dwordx4 v[174:177], v254, s[24:27], s12 offen nt
	s_add_u32 s12, s12, 0x12c000
	s_add_u32 s32, s32, 0x40000
	s_mov_b32 s19, 0x80000000
	buffer_store_dwordx4 v[226:229], v246, s[28:31], s19 offen nt
	s_mov_b32 s10, 1
	global_load_dwordx4 v[2:5], v236, s[4:5]
	global_load_dwordx4 v[6:9], v236, s[4:5] offset:1024
	v_add_u32_e32 v236, 0x2000, v236
	global_load_dwordx4 v[10:13], v236, s[4:5]
	global_load_dwordx4 v[14:17], v236, s[4:5] offset:1024
	v_add_u32_e32 v236, 0x2000, v236
	global_load_dwordx4 v[18:21], v236, s[4:5]
	global_load_dwordx4 v[22:25], v236, s[4:5] offset:1024
	v_add_u32_e32 v236, 0x2000, v236
	global_load_dwordx4 v[26:29], v236, s[4:5]
	global_load_dwordx4 v[30:33], v236, s[4:5] offset:1024
	v_add_u32_e32 v236, 0x2000, v236
	global_load_dwordx4 v[34:37], v236, s[4:5]
	global_load_dwordx4 v[38:41], v236, s[4:5] offset:1024
	v_add_u32_e32 v236, 0x2000, v236
	global_load_dwordx4 v[42:45], v236, s[4:5]
	global_load_dwordx4 v[46:49], v236, s[4:5] offset:1024
	v_add_u32_e32 v236, 0x2000, v236
	global_load_dwordx4 v[50:53], v236, s[4:5]
	global_load_dwordx4 v[54:57], v236, s[4:5] offset:1024
	v_add_u32_e32 v236, 0x2000, v236
	global_load_dwordx4 v[58:61], v236, s[4:5]
	global_load_dwordx4 v[62:65], v236, s[4:5] offset:1024
	v_add_u32_e32 v236, 0x2000, v236
	global_load_dwordx4 v[66:69], v236, s[4:5]
	global_load_dwordx4 v[70:73], v236, s[4:5] offset:1024
	v_add_u32_e32 v236, 0x2000, v236
	global_load_dwordx4 v[74:77], v236, s[4:5]
	global_load_dwordx4 v[78:81], v236, s[4:5] offset:1024
	v_add_u32_e32 v236, 0x2000, v236
	global_load_dwordx4 v[82:85], v236, s[4:5]
	global_load_dwordx4 v[86:89], v236, s[4:5] offset:1024
	v_add_u32_e32 v236, 0x2000, v236
	global_load_dwordx4 v[90:93], v236, s[4:5]
	global_load_dwordx4 v[94:97], v236, s[4:5] offset:1024
	v_add_u32_e32 v236, 0x2000, v236
	global_load_dwordx4 v[98:101], v236, s[4:5]
	global_load_dwordx4 v[102:105], v236, s[4:5] offset:1024
	v_add_u32_e32 v236, 0x2000, v236
	global_load_dwordx4 v[106:109], v236, s[4:5]
	global_load_dwordx4 v[110:113], v236, s[4:5] offset:1024
	v_add_u32_e32 v236, 0x2000, v236
	global_load_dwordx4 v[114:117], v236, s[4:5]
	global_load_dwordx4 v[118:121], v236, s[4:5] offset:1024
	v_add_u32_e32 v236, 0x2000, v236
	global_load_dwordx4 v[122:125], v236, s[4:5]
	global_load_dwordx4 v[126:129], v236, s[4:5] offset:1024
	v_add_u32_e32 v236, 0x2000, v236
	global_load_dwordx4 v[130:133], v236, s[4:5]
	global_load_dwordx4 v[134:137], v236, s[4:5] offset:1024
	s_waitcnt vmcnt(45)
	ds_write_b128 v248, v[178:181]
	ds_write_b128 v248, v[182:185] offset:1024
	ds_write_b128 v248, v[186:189] offset:2048
	ds_write_b128 v248, v[190:193] offset:3072
	s_waitcnt lgkmcnt(0)
	s_barrier
	s_branch .Lg_half1
.Lg_top:
	v_readlane_b32 s13, v247, s10
	s_add_u32 s14, s12, 0x4b0
	s_add_u32 s15, s12, 0x960
	s_add_u32 s16, s12, 0xe10
	s_nop 1
	s_and_b32 s18, s13, 0xff
	s_cmp_eq_u32 s18, 1
	s_cselect_b32 s42, s12, 0x80000000
	s_and_b32 s18, s13, 0xff00
	s_cmp_eq_u32 s18, 0x100
	s_cselect_b32 s14, s14, 0x80000000
	s_and_b32 s18, s13, 0xff0000
	s_cmp_eq_u32 s18, 0x10000
	s_cselect_b32 s15, s15, 0x80000000
	s_and_b32 s18, s13, 0xff000000
	s_cmp_eq_u32 s18, 0x1000000
	s_cselect_b32 s16, s16, 0x80000000
	v_lshrrev_b32_e64 v249, v240, s13
	v_and_b32_e32 v249, 0xff, v249
	v_cmp_eq_u32_e32 vcc, 1, v249
	s_nop 1
	v_cndmask_b32_e32 v254, v255, v239, vcc
	s_sub_u32 s18, s10, 2
	s_cmp_lt_u32 s18, s9
	s_cbranch_scc0 .Lg_s2skip0
	s_waitcnt vmcnt(21)
	v_cvt_pk_f16_f32 v250, v138, v139
	v_cvt_pk_f16_f32 v251, v140, v141
	ds_write_b64 v241, v[250:251] offset:0
	buffer_load_dwordx4 v[138:141], v238, s[20:23], s42 offen nt
	s_waitcnt vmcnt(21)
	v_cvt_pk_f16_f32 v252, v142, v143
	v_cvt_pk_f16_f32 v253, v144, v145
	ds_write_b64 v241, v[252:253] offset:600
	buffer_load_dwordx4 v[142:145], v238, s[24:27], s42 offen nt
	s_waitcnt vmcnt(21)
	v_cvt_pk_f16_f32 v250, v146, v147
	v_cvt_pk_f16_f32 v251, v148, v149
	ds_write_b64 v241, v[250:251] offset:1248
	buffer_load_dwordx4 v[146:149], v238, s[20:23], s14 offen nt
	s_waitcnt vmcnt(21)
	v_cvt_pk_f16_f32 v252, v150, v151
	v_cvt_pk_f16_f32 v253, v152, v153
	ds_write_b64 v241, v[252:253] offset:1848
	buffer_load_dwordx4 v[150:153], v238, s[24:27], s14 offen nt
	s_waitcnt vmcnt(21)
	v_cvt_pk_f16_f32 v250, v154, v155
	v_cvt_pk_f16_f32 v251, v156, v157
	ds_write_b64 v241, v[250:251] offset:2496
	buffer_load_dwordx4 v[154:157], v238, s[20:23], s15 offen nt
	s_waitcnt vmcnt(21)
	v_cvt_pk_f16_f32 v252, v158, v159
	v_cvt_pk_f16_f32 v253, v160, v161
	ds_write_b64 v241, v[252:253] offset:3096
	buffer_load_dwordx4 v[158:161], v238, s[24:27], s15 offen nt
	s_waitcnt vmcnt(21)
	v_cvt_pk_f16_f32 v250, v162, v163
	v_cvt_pk_f16_f32 v251, v164, v165
	ds_write_b64 v241, v[250:251] offset:3744
	buffer_load_dwordx4 v[162:165], v238, s[20:23], s16 offen nt
	s_waitcnt vmcnt(21)
	v_cvt_pk_f16_f32 v252, v166, v167
	v_cvt_pk_f16_f32 v253, v168, v169
	ds_write_b64 v241, v[252:253] offset:4344
	buffer_load_dwordx4 v[166:169], v238, s[24:27], s16 offen nt
	s_mov_b64 exec, s[34:35]
	s_waitcnt vmcnt(21)
	v_cvt_pk_f16_f32 v250, v170, v171
	v_cvt_pk_f16_f32 v251, v172, v173
	ds_write_b64 v242, v[250:251] offset:0
	s_mov_b64 exec, -1
	buffer_load_dwordx4 v[170:173], v254, s[20:23], s12 offen nt
	s_mov_b64 exec, s[34:35]
	s_waitcnt vmcnt(21)
	v_cvt_pk_f16_f32 v252, v174, v175
	v_cvt_pk_f16_f32 v253, v176, v177
	ds_write_b64 v242, v[252:253] offset:600
	s_mov_b64 exec, -1
	buffer_load_dwordx4 v[174:177], v254, s[24:27], s12 offen nt
	s_branch .Lg_s1done0
.Lg_s2skip0:
	buffer_load_dwordx4 v[138:141], v238, s[20:23], s42 offen nt
	buffer_load_dwordx4 v[142:145], v238, s[24:27], s42 offen nt
	buffer_load_dwordx4 v[146:149], v238, s[20:23], s14 offen nt
	buffer_load_dwordx4 v[150:153], v238, s[24:27], s14 offen nt
	buffer_load_dwordx4 v[154:157], v238, s[20:23], s15 offen nt
	buffer_load_dwordx4 v[158:161], v238, s[24:27], s15 offen nt
	buffer_load_dwordx4 v[162:165], v238, s[20:23], s16 offen nt
	buffer_load_dwordx4 v[166:169], v238, s[24:27], s16 offen nt
	buffer_load_dwordx4 v[170:173], v254, s[20:23], s12 offen nt
	buffer_load_dwordx4 v[174:177], v254, s[24:27], s12 offen nt
.Lg_s1done0:
	s_add_u32 s12, s12, 0x12c000
	s_sub_u32 s18, s10, 3
	s_cmp_lt_u32 s18, s9
	s_cbranch_scc0 .Lg_s3skip0
	ds_read_b128 v[226:229], v243 offset:21056
	ds_read_b128 v[230:233], v248
	ds_read_b128 v[234:237], v248 offset:1024
	s_waitcnt lgkmcnt(0)
	v_mfma_f32_16x16x32_f16 v[218:221], v[226:229], v[230:233], 0
	v_mfma_f32_16x16x32_f16 v[222:225], v[226:229], v[234:237], 0
	ds_read_b128 v[226:229], v243 offset:21120
	ds_read_b128 v[230:233], v248 offset:2048
	ds_read_b128 v[234:237], v248 offset:3072
	s_waitcnt lgkmcnt(0)
	v_mfma_f32_16x16x32_f16 v[218:221], v[226:229], v[230:233], v[218:221]
	v_mfma_f32_16x16x32_f16 v[222:225], v[226:229], v[234:237], v[222:225]
	ds_read_b128 v[226:229], v243 offset:19968
	ds_read_b128 v[230:233], v243 offset:20032
	ds_read_b128 v[234:237], v243 offset:20096
	s_waitcnt lgkmcnt(2)
	v_mfma_f32_16x16x32_f16 v[218:221], v[226:229], v[2:5], v[218:221]
	v_mfma_f32_16x16x32_f16 v[222:225], v[226:229], v[6:9], v[222:225]
	ds_read_b128 v[226:229], v243 offset:20160
	s_waitcnt lgkmcnt(2)
	v_mfma_f32_16x16x32_f16 v[218:221], v[230:233], v[10:13], v[218:221]
	v_mfma_f32_16x16x32_f16 v[222:225], v[230:233], v[14:17], v[222:225]
	ds_read_b128 v[230:233], v243 offset:20224
	s_waitcnt lgkmcnt(2)
	v_mfma_f32_16x16x32_f16 v[218:221], v[234:237], v[18:21], v[218:221]
	v_mfma_f32_16x16x32_f16 v[222:225], v[234:237], v[22:25], v[222:225]
	ds_read_b128 v[234:237], v243 offset:20288
	s_waitcnt lgkmcnt(2)
	v_mfma_f32_16x16x32_f16 v[218:221], v[226:229], v[26:29], v[218:221]
	v_mfma_f32_16x16x32_f16 v[222:225], v[226:229], v[30:33], v[222:225]
	ds_read_b128 v[226:229], v243 offset:20352
	s_waitcnt lgkmcnt(2)
	v_mfma_f32_16x16x32_f16 v[218:221], v[230:233], v[34:37], v[218:221]
	v_mfma_f32_16x16x32_f16 v[222:225], v[230:233], v[38:41], v[222:225]
	ds_read_b128 v[230:233], v243 offset:20416
	s_waitcnt lgkmcnt(2)
	v_mfma_f32_16x16x32_f16 v[218:221], v[234:237], v[42:45], v[218:221]
	v_mfma_f32_16x16x32_f16 v[222:225], v[234:237], v[46:49], v[222:225]
	ds_read_b128 v[234:237], v243 offset:20480
	s_waitcnt lgkmcnt(2)
	v_mfma_f32_16x16x32_f16 v[218:221], v[226:229], v[50:53], v[218:221]
	v_mfma_f32_16x16x32_f16 v[222:225], v[226:229], v[54:57], v[222:225]
	ds_read_b128 v[226:229], v243 offset:20544
	s_waitcnt lgkmcnt(2)
	v_mfma_f32_16x16x32_f16 v[218:221], v[230:233], v[58:61], v[218:221]
	v_mfma_f32_16x16x32_f16 v[222:225], v[230:233], v[62:65], v[222:225]
	ds_read_b128 v[230:233], v243 offset:20608
	s_waitcnt lgkmcnt(2)
	v_mfma_f32_16x16x32_f16 v[218:221], v[234:237], v[66:69], v[218:221]
	v_mfma_f32_16x16x32_f16 v[222:225], v[234:237], v[70:73], v[222:225]
	ds_read_b128 v[234:237], v243 offset:20672
	s_waitcnt lgkmcnt(2)
	v_mfma_f32_16x16x32_f16 v[218:221], v[226:229], v[74:77], v[218:221]
	v_mfma_f32_16x16x32_f16 v[222:225], v[226:229], v[78:81], v[222:225]
	ds_read_b128 v[226:229], v243 offset:20736
	s_waitcnt lgkmcnt(2)
	v_mfma_f32_16x16x32_f16 v[218:221], v[230:233], v[82:85], v[218:221]
	v_mfma_f32_16x16x32_f16 v[222:225], v[230:233], v[86:89], v[222:225]
	ds_read_b128 v[230:233], v243 offset:20800
	s_waitcnt lgkmcnt(2)
	v_mfma_f32_16x16x32_f16 v[218:221], v[234:237], v[90:93], v[218:221]
	v_mfma_f32_16x16x32_f16 v[222:225], v[234:237], v[94:97], v[222:225]
	ds_read_b128 v[234:237], v243 offset:20864
	s_waitcnt lgkmcnt(2)
	v_mfma_f32_16x16x32_f16 v[218:221], v[226:229], v[98:101], v[218:221]
	v_mfma_f32_16x16x32_f16 v[222:225], v[226:229], v[102:105], v[222:225]
	ds_read_b128 v[226:229], v243 offset:20928
	s_waitcnt lgkmcnt(2)
	v_mfma_f32_16x16x32_f16 v[218:221], v[230:233], v[106:109], v[218:221]
	v_mfma_f32_16x16x32_f16 v[222:225], v[230:233], v[110:113], v[222:225]
	ds_read_b128 v[230:233], v243 offset:20992
	s_waitcnt lgkmcnt(2)
	v_mfma_f32_16x16x32_f16 v[218:221], v[234:237], v[114:117], v[218:221]
	v_mfma_f32_16x16x32_f16 v[222:225], v[234:237], v[118:121], v[222:225]
	s_waitcnt lgkmcnt(1)
	v_mfma_f32_16x16x32_f16 v[218:221], v[226:229], v[122:125], v[218:221]
	v_mfma_f32_16x16x32_f16 v[222:225], v[226:229], v[126:129], v[222:225]
	s_waitcnt lgkmcnt(0)
	v_mfma_f32_16x16x32_f16 v[218:221], v[230:233], v[130:133], v[218:221]
	v_mfma_f32_16x16x32_f16 v[222:225], v[230:233], v[134:137], v[222:225]
	s_nop 7
	s_nop 3
	v_cvt_f16_f32_e32 v249, v218
	v_cvt_f16_f32_e32 v250, v219
	v_cvt_f16_f32_e32 v251, v220
	v_cvt_f16_f32_e32 v252, v221
	ds_write_b16 v244, v249 offset:4352
	ds_write_b16 v244, v250 offset:4624
	ds_write_b16 v244, v251 offset:4896
	ds_write_b16 v244, v252 offset:5168
	v_cvt_f16_f32_e32 v249, v222
	v_cvt_f16_f32_e32 v250, v223
	v_cvt_f16_f32_e32 v251, v224
	v_cvt_f16_f32_e32 v252, v225
	ds_write_b16 v244, v249 offset:4384
	ds_write_b16 v244, v250 offset:4656
	ds_write_b16 v244, v251 offset:4928
	ds_write_b16 v244, v252 offset:5200

.Lg_half1:
	v_readlane_b32 s13, v247, s10
	s_add_u32 s14, s12, 0x4b0
	s_add_u32 s15, s12, 0x960
	s_add_u32 s16, s12, 0xe10
	s_nop 1
	s_and_b32 s18, s13, 0xff
	s_cmp_eq_u32 s18, 1
	s_cselect_b32 s42, s12, 0x80000000
	s_and_b32 s18, s13, 0xff00
	s_cmp_eq_u32 s18, 0x100
	s_cselect_b32 s14, s14, 0x80000000
	s_and_b32 s18, s13, 0xff0000
	s_cmp_eq_u32 s18, 0x10000
	s_cselect_b32 s15, s15, 0x80000000
	s_and_b32 s18, s13, 0xff000000
	s_cmp_eq_u32 s18, 0x1000000
	s_cselect_b32 s16, s16, 0x80000000
	v_lshrrev_b32_e64 v249, v240, s13
	v_and_b32_e32 v249, 0xff, v249
	v_cmp_eq_u32_e32 vcc, 1, v249
	s_nop 1
	v_cndmask_b32_e32 v254, v255, v239, vcc
	s_sub_u32 s18, s10, 2
	s_cmp_lt_u32 s18, s9
	s_cbranch_scc0 .Lg_s2skip1
	s_waitcnt vmcnt(21)
	v_cvt_pk_f16_f32 v250, v178, v179
	v_cvt_pk_f16_f32 v251, v180, v181
	ds_write_b64 v241, v[250:251] offset:19968
	buffer_load_dwordx4 v[178:181], v238, s[20:23], s42 offen nt
	s_waitcnt vmcnt(21)
	v_cvt_pk_f16_f32 v252, v182, v183
	v_cvt_pk_f16_f32 v253, v184, v185
	ds_write_b64 v241, v[252:253] offset:20568
	buffer_load_dwordx4 v[182:185], v238, s[24:27], s42 offen nt
	s_waitcnt vmcnt(21)
	v_cvt_pk_f16_f32 v250, v186, v187
	v_cvt_pk_f16_f32 v251, v188, v189
	ds_write_b64 v241, v[250:251] offset:21216
	buffer_load_dwordx4 v[186:189], v238, s[20:23], s14 offen nt
	s_waitcnt vmcnt(21)
	v_cvt_pk_f16_f32 v252, v190, v191
	v_cvt_pk_f16_f32 v253, v192, v193
	ds_write_b64 v241, v[252:253] offset:21816
	buffer_load_dwordx4 v[190:193], v238, s[24:27], s14 offen nt
	s_waitcnt vmcnt(21)
	v_cvt_pk_f16_f32 v250, v194, v195
	v_cvt_pk_f16_f32 v251, v196, v197
	ds_write_b64 v241, v[250:251] offset:22464
	buffer_load_dwordx4 v[194:197], v238, s[20:23], s15 offen nt
	s_waitcnt vmcnt(21)
	v_cvt_pk_f16_f32 v252, v198, v199
	v_cvt_pk_f16_f32 v253, v200, v201
	ds_write_b64 v241, v[252:253] offset:23064
	buffer_load_dwordx4 v[198:201], v238, s[24:27], s15 offen nt
	s_waitcnt vmcnt(21)
	v_cvt_pk_f16_f32 v250, v202, v203
	v_cvt_pk_f16_f32 v251, v204, v205
	ds_write_b64 v241, v[250:251] offset:23712
	buffer_load_dwordx4 v[202:205], v238, s[20:23], s16 offen nt
	s_waitcnt vmcnt(21)
	v_cvt_pk_f16_f32 v252, v206, v207
	v_cvt_pk_f16_f32 v253, v208, v209
	ds_write_b64 v241, v[252:253] offset:24312
	buffer_load_dwordx4 v[206:209], v238, s[24:27], s16 offen nt
	s_mov_b64 exec, s[34:35]
	s_waitcnt vmcnt(21)
	v_cvt_pk_f16_f32 v250, v210, v211
	v_cvt_pk_f16_f32 v251, v212, v213
	ds_write_b64 v242, v[250:251] offset:19968
	s_mov_b64 exec, -1
	buffer_load_dwordx4 v[210:213], v254, s[20:23], s12 offen nt
	s_mov_b64 exec, s[34:35]
	s_waitcnt vmcnt(21)
	v_cvt_pk_f16_f32 v252, v214, v215
	v_cvt_pk_f16_f32 v253, v216, v217
	ds_write_b64 v242, v[252:253] offset:20568
	s_mov_b64 exec, -1
	buffer_load_dwordx4 v[214:217], v254, s[24:27], s12 offen nt
	s_branch .Lg_s1done1
.Lg_s2skip1:
	buffer_load_dwordx4 v[178:181], v238, s[20:23], s42 offen nt
	buffer_load_dwordx4 v[182:185], v238, s[24:27], s42 offen nt
	buffer_load_dwordx4 v[186:189], v238, s[20:23], s14 offen nt
	buffer_load_dwordx4 v[190:193], v238, s[24:27], s14 offen nt
	buffer_load_dwordx4 v[194:197], v238, s[20:23], s15 offen nt
	buffer_load_dwordx4 v[198:201], v238, s[24:27], s15 offen nt
	buffer_load_dwordx4 v[202:205], v238, s[20:23], s16 offen nt
	buffer_load_dwordx4 v[206:209], v238, s[24:27], s16 offen nt
	buffer_load_dwordx4 v[210:213], v254, s[20:23], s12 offen nt
	buffer_load_dwordx4 v[214:217], v254, s[24:27], s12 offen nt
.Lg_s1done1:
	s_add_u32 s12, s12, 0x12c000
	s_sub_u32 s18, s10, 3
	s_cmp_lt_u32 s18, s9
	s_cbranch_scc0 .Lg_s3skip1
	ds_read_b128 v[226:229], v243 offset:1088
	ds_read_b128 v[230:233], v248
	ds_read_b128 v[234:237], v248 offset:1024
	s_waitcnt lgkmcnt(0)
	v_mfma_f32_16x16x32_f16 v[218:221], v[226:229], v[230:233], 0
	v_mfma_f32_16x16x32_f16 v[222:225], v[226:229], v[234:237], 0
	ds_read_b128 v[226:229], v243 offset:1152
	ds_read_b128 v[230:233], v248 offset:2048
	ds_read_b128 v[234:237], v248 offset:3072
	s_waitcnt lgkmcnt(0)
	v_mfma_f32_16x16x32_f16 v[218:221], v[226:229], v[230:233], v[218:221]
	v_mfma_f32_16x16x32_f16 v[222:225], v[226:229], v[234:237], v[222:225]
	ds_read_b128 v[226:229], v243 offset:0
	ds_read_b128 v[230:233], v243 offset:64
	ds_read_b128 v[234:237], v243 offset:128
	s_waitcnt lgkmcnt(2)
	v_mfma_f32_16x16x32_f16 v[218:221], v[226:229], v[2:5], v[218:221]
	v_mfma_f32_16x16x32_f16 v[222:225], v[226:229], v[6:9], v[222:225]
	ds_read_b128 v[226:229], v243 offset:192
	s_waitcnt lgkmcnt(2)
	v_mfma_f32_16x16x32_f16 v[218:221], v[230:233], v[10:13], v[218:221]
	v_mfma_f32_16x16x32_f16 v[222:225], v[230:233], v[14:17], v[222:225]
	ds_read_b128 v[230:233], v243 offset:256
	s_waitcnt lgkmcnt(2)
	v_mfma_f32_16x16x32_f16 v[218:221], v[234:237], v[18:21], v[218:221]
	v_mfma_f32_16x16x32_f16 v[222:225], v[234:237], v[22:25], v[222:225]
	ds_read_b128 v[234:237], v243 offset:320
	s_waitcnt lgkmcnt(2)
	v_mfma_f32_16x16x32_f16 v[218:221], v[226:229], v[26:29], v[218:221]
	v_mfma_f32_16x16x32_f16 v[222:225], v[226:229], v[30:33], v[222:225]
	ds_read_b128 v[226:229], v243 offset:384
	s_waitcnt lgkmcnt(2)
	v_mfma_f32_16x16x32_f16 v[218:221], v[230:233], v[34:37], v[218:221]
	v_mfma_f32_16x16x32_f16 v[222:225], v[230:233], v[38:41], v[222:225]
	ds_read_b128 v[230:233], v243 offset:448
	s_waitcnt lgkmcnt(2)
	v_mfma_f32_16x16x32_f16 v[218:221], v[234:237], v[42:45], v[218:221]
	v_mfma_f32_16x16x32_f16 v[222:225], v[234:237], v[46:49], v[222:225]
	ds_read_b128 v[234:237], v243 offset:512
	s_waitcnt lgkmcnt(2)
	v_mfma_f32_16x16x32_f16 v[218:221], v[226:229], v[50:53], v[218:221]
	v_mfma_f32_16x16x32_f16 v[222:225], v[226:229], v[54:57], v[222:225]
	ds_read_b128 v[226:229], v243 offset:576
	s_waitcnt lgkmcnt(2)
	v_mfma_f32_16x16x32_f16 v[218:221], v[230:233], v[58:61], v[218:221]
	v_mfma_f32_16x16x32_f16 v[222:225], v[230:233], v[62:65], v[222:225]
	ds_read_b128 v[230:233], v243 offset:640
	s_waitcnt lgkmcnt(2)
	v_mfma_f32_16x16x32_f16 v[218:221], v[234:237], v[66:69], v[218:221]
	v_mfma_f32_16x16x32_f16 v[222:225], v[234:237], v[70:73], v[222:225]
	ds_read_b128 v[234:237], v243 offset:704
	s_waitcnt lgkmcnt(2)
	v_mfma_f32_16x16x32_f16 v[218:221], v[226:229], v[74:77], v[218:221]
	v_mfma_f32_16x16x32_f16 v[222:225], v[226:229], v[78:81], v[222:225]
	ds_read_b128 v[226:229], v243 offset:768
	s_waitcnt lgkmcnt(2)
	v_mfma_f32_16x16x32_f16 v[218:221], v[230:233], v[82:85], v[218:221]
	v_mfma_f32_16x16x32_f16 v[222:225], v[230:233], v[86:89], v[222:225]
	ds_read_b128 v[230:233], v243 offset:832
	s_waitcnt lgkmcnt(2)
	v_mfma_f32_16x16x32_f16 v[218:221], v[234:237], v[90:93], v[218:221]
	v_mfma_f32_16x16x32_f16 v[222:225], v[234:237], v[94:97], v[222:225]
	ds_read_b128 v[234:237], v243 offset:896
	s_waitcnt lgkmcnt(2)
	v_mfma_f32_16x16x32_f16 v[218:221], v[226:229], v[98:101], v[218:221]
	v_mfma_f32_16x16x32_f16 v[222:225], v[226:229], v[102:105], v[222:225]
	ds_read_b128 v[226:229], v243 offset:960
	s_waitcnt lgkmcnt(2)
	v_mfma_f32_16x16x32_f16 v[218:221], v[230:233], v[106:109], v[218:221]
	v_mfma_f32_16x16x32_f16 v[222:225], v[230:233], v[110:113], v[222:225]
	ds_read_b128 v[230:233], v243 offset:1024
	s_waitcnt lgkmcnt(2)
	v_mfma_f32_16x16x32_f16 v[218:221], v[234:237], v[114:117], v[218:221]
	v_mfma_f32_16x16x32_f16 v[222:225], v[234:237], v[118:121], v[222:225]
	s_waitcnt lgkmcnt(1)
	v_mfma_f32_16x16x32_f16 v[218:221], v[226:229], v[122:125], v[218:221]
	v_mfma_f32_16x16x32_f16 v[222:225], v[226:229], v[126:129], v[222:225]
	s_waitcnt lgkmcnt(0)
	v_mfma_f32_16x16x32_f16 v[218:221], v[230:233], v[130:133], v[218:221]
	v_mfma_f32_16x16x32_f16 v[222:225], v[230:233], v[134:137], v[222:225]
	s_nop 7
	s_nop 3
	v_cvt_f16_f32_e32 v249, v218
	v_cvt_f16_f32_e32 v250, v219
	v_cvt_f16_f32_e32 v251, v220
	v_cvt_f16_f32_e32 v252, v221
	ds_write_b16 v244, v249 offset:0
	ds_write_b16 v244, v250 offset:272
	ds_write_b16 v244, v251 offset:544
	ds_write_b16 v244, v252 offset:816
	v_cvt_f16_f32_e32 v249, v222
	v_cvt_f16_f32_e32 v250, v223
	v_cvt_f16_f32_e32 v251, v224
	v_cvt_f16_f32_e32 v252, v225
	ds_write_b16 v244, v249 offset:32
	ds_write_b16 v244, v250 offset:304
	ds_write_b16 v244, v251 offset:576
	ds_write_b16 v244, v252 offset:848
